# v57 + moe1 first unit: the four gathered-row offset loads issued together with one wait
# baseline (speedup 1.0000x reference)
; #define LAS __attribute__((address_space(3)))
; #define PG8_STAGE(bufoff, gbase, voff) do { _Pragma("unroll") for (int _i = 0; _i < 2; ++_i) \
;         __builtin_amdgcn_global_load_lds((const unsigned*)((const char*)(gbase) + (voff)[_i]), (LAS unsigned*)(lds + (bufoff) + ldsw + _i * 8192), 16, 0, 0); } while (0)
; #define PG8_AOFFS(dst, U) do { int t2_ = tid; asm volatile("" : "+v"(t2_)); _Pragma("unroll") for (int i = 0; i < 2; ++i) { int R, C; stage_rc(t2_ * 16 + i * 8192, R, C); \
;         dst[0][i] = S.a_off(U, R) + (unsigned)C * 2u; dst[1][i] = S.a_off(U, HALF + R) + (unsigned)C * 2u; } } while (0)
;     __device__ __forceinline__ unsigned a_off(const Unit& u, int r) const { return (unsigned)(u.pm * 256 + r) * (unsigned)(K * 2); }
; template <class Epi, class Sched>
; __device__ __forceinline__ void gemm_phase(LAS unsigned char* lds, const int tid, const char* Abase, const int K, const Sched& S, const Epi& E) {
;     ...
;     PG8_AOFFS(vc, cur);
;     const char* cB = S.b_tile(cur);
;     E.begin(cur, ui, tid, lds);
;     PG8_STAGE(PG8_SB(0, 0), cB, voffB); PG8_STAGE(PG8_SB(0, 1), cB + hstep, voffB); PG8_STAGE(PG8_SA(0, 0), Abase, vc[0]); PG8_STAGE(PG8_SA(0, 1), Abase, vc[1]);
;     __device__ __forceinline__ unsigned a_off(const Unit& u, int r) const {
;         if (gather) { int tok = 0; if (r < u.nrows) tok = liste[(size_t)u.e * T + 256 * u.tile + r] >> 1; return (unsigned)tok * (unsigned)(K * 2); }
;     EPI_NOMID
;     __device__ __forceinline__ void begin(const Unit& u, int ui, int tid, LAS unsigned char* lds) const {
;         if (tid < 256) { float rs = 0.f; if (tid < u.nrows) rs = RS[liste[(size_t)u.e * T + 256 * u.tile + tid] >> 1]; rtab_put(lds, ui, tid, rs, 0.f); } }
.LBB0_1141:
	s_andn2_b64 vcc, exec, s[10:11]
	s_cbranch_vccnz .LBB0_1217
	v_mov_b32_e32 v4, v188
	v_lshlrev_b32_e32 v2, 8, v0
	v_ashrrev_i32_e32 v0, 31, v4
	v_lshrrev_b32_e32 v0, 26, v0
	v_add_u32_e32 v0, v4, v0
	v_ashrrev_i32_e32 v7, 6, v0
	v_bfe_i32 v0, v4, 27, 1
	v_lshlrev_b32_e32 v12, 4, v4
	v_lshrrev_b32_e32 v0, 22, v0
	v_add_u32_e32 v0, v12, v0
	v_and_b32_e32 v0, 0xfffffc00, v0
	v_sub_u32_e32 v0, v12, v0
	v_lshrrev_b32_e32 v4, 4, v0
	v_bitop3_b32 v8, v4, v0, 32 bitop3:0x6c
	s_add_u32 s2, s74, 0x800000
	v_ashrrev_i32_e32 v4, 31, v8
	s_addc_u32 s33, s75, 0
	s_ashr_i32 s13, s12, 31
	v_lshrrev_b32_e32 v4, 26, v4
	s_lshl_b64 s[6:7], s[12:13], 17
	v_lshlrev_b32_e32 v0, 3, v7
	v_add_u32_e32 v4, v8, v4
	v_ashrrev_i32_e32 v3, 31, v2
	s_add_u32 s6, s2, s6
	v_and_b32_e32 v0, -16, v0
	v_ashrrev_i32_e32 v9, 6, v4
	s_addc_u32 s7, s33, s7
	v_lshlrev_b64 v[2:3], 2, v[2:3]
	v_add_u32_e32 v4, v9, v0
	v_lshl_add_u64 v[2:3], s[6:7], 0, v[2:3]
	v_cmp_lt_i32_e32 vcc, v4, v153
	v_mov_b32_e32 v10, 0
	v_ashrrev_i32_e32 v5, 31, v4
	v_mov_b32_e32 v11, 0
	v_mov_b32_e32 v240, 0
	v_mov_b32_e32 v241, 0
	v_mov_b32_e32 v242, 0
	v_mov_b32_e32 v243, 0
	s_and_saveexec_b64 s[10:11], vcc
	s_cbranch_execz .LBB0_1144
	v_lshl_add_u64 v[14:15], v[4:5], 2, v[2:3]
	flat_load_dword v240, v[14:15]
.LBB0_1144:
	s_or_b64 exec, exec, s[10:11]
	v_add_u32_e32 v0, 0x80, v4
	v_cmp_lt_i32_e32 vcc, v0, v153
	s_and_saveexec_b64 s[10:11], vcc
	s_cbranch_execz .LBB0_1146
	v_lshl_add_u64 v[4:5], v[4:5], 2, v[2:3]
	flat_load_dword v241, v[4:5] offset:512
.LBB0_1146:
	s_or_b64 exec, exec, s[10:11]
	v_add_u32_e32 v0, 0x2000, v12
	v_ashrrev_i32_e32 v4, 31, v0
	v_lshrrev_b32_e32 v4, 22, v4
	v_add_u32_e32 v4, v0, v4
	v_ashrrev_i32_e32 v12, 10, v4
	v_mul_i32_i24_e32 v4, 0x400, v12
	v_sub_u32_e32 v0, v0, v4
	v_lshrrev_b32_e32 v4, 4, v0
	v_bitop3_b32 v14, v4, v0, 32 bitop3:0x6c
	v_ashrrev_i32_e32 v4, 31, v14
	v_lshrrev_b32_e32 v4, 26, v4
	v_lshlrev_b32_e32 v0, 3, v12
	v_add_u32_e32 v4, v14, v4
	v_and_b32_e32 v0, -16, v0
	v_ashrrev_i32_e32 v15, 6, v4
	v_add_u32_e32 v4, v15, v0
	v_cmp_lt_i32_e32 vcc, v4, v153
	v_mov_b32_e32 v16, 0
	v_ashrrev_i32_e32 v5, 31, v4
	v_mov_b32_e32 v13, 0
	s_and_saveexec_b64 s[10:11], vcc
	s_cbranch_execz .LBB0_1148
	v_lshl_add_u64 v[18:19], v[4:5], 2, v[2:3]
	flat_load_dword v242, v[18:19]
.LBB0_1148:
	s_or_b64 exec, exec, s[10:11]
	v_add_u32_e32 v0, 0x80, v4
	v_cmp_lt_i32_e32 vcc, v0, v153
	s_and_saveexec_b64 s[10:11], vcc
	s_cbranch_execz .LBB0_1150
	v_lshl_add_u64 v[4:5], v[4:5], 2, v[2:3]
	flat_load_dword v243, v[4:5] offset:512
.LBB0_1150:
	s_or_b64 exec, exec, s[10:11]
	s_waitcnt vmcnt(0) lgkmcnt(0)
	v_lshlrev_b32_e32 v240, 10, v240
	v_lshlrev_b32_e32 v241, 10, v241
	v_lshlrev_b32_e32 v242, 10, v242
	v_lshlrev_b32_e32 v243, 10, v243
	v_and_b32_e32 v11, 0xfffff800, v240
	v_and_b32_e32 v10, 0xfffff800, v241
	v_and_b32_e32 v13, 0xfffff800, v242
	v_and_b32_e32 v16, 0xfffff800, v243
	s_add_u32 s14, s74, 0x500000
	s_movk_i32 s6, 0x100
	s_addc_u32 s15, s75, 0
	v_cmp_gt_i32_e64 s[10:11], s6, v188
	s_and_saveexec_b64 s[6:7], s[10:11]
	s_xor_b64 s[18:19], exec, s[6:7]
	s_cbranch_execz .LBB0_1154
	v_cmp_lt_i32_e32 vcc, v188, v153
	v_mov_b32_e32 v0, 0
	s_and_saveexec_b64 s[20:21], vcc
	s_cbranch_execz .LBB0_1153
	v_ashrrev_i32_e32 v189, 31, v188
	v_lshl_add_u64 v[2:3], v[188:189], 2, v[2:3]
	flat_load_dword v0, v[2:3]
	s_waitcnt vmcnt(0) lgkmcnt(0)
	v_ashrrev_i32_e32 v2, 1, v0
	v_ashrrev_i32_e32 v3, 31, v2
	v_lshl_add_u64 v[2:3], v[2:3], 2, s[14:15]
	flat_load_dword v0, v[2:3]
